# G=200; dedicated converters 6880 W1 tiles; GEMM-in epilogues convert 800 tiles (half workgroup per unit); W_out-GEMM epilogues 512 tiles; GEMM1 epilogues 3200 W2 tiles
# baseline (speedup 1.0000x reference)
.LBB0_86:
	s_cmp_lt_i32 s50, 2
	s_cselect_b64 s[6:7], -1, 0
	s_and_b64 s[0:1], s[6:7], s[2:3]
	s_andn2_b64 vcc, exec, s[0:1]
	v_writelane_b32 v254, s60, 4
	s_cbranch_vccnz .LBB0_260
	s_mov_b64 s[2:3], s[80:81]
	s_load_dwordx2 s[8:9], s[2:3], 0xa8
	s_cmpk_lg_i32 s56, 0x100
	s_cselect_b32 s0, s56, 0xc8
	s_cmp_ge_i32 s78, s0
	s_mov_b64 s[4:5], -1
	s_cbranch_scc0 .LBB0_145
	s_sub_i32 s1, s78, s0
	s_cmpk_gt_i32 s1, 0x1adf
	s_cbranch_scc1 .LBB0_144
	s_sub_i32 s20, s56, s0
	s_abs_i32 s4, s20
	v_cvt_f32_u32_e32 v1, s4
	s_load_dwordx2 s[10:11], s[2:3], 0x78
	s_load_dwordx2 s[12:13], s[2:3], 0x88
	s_sub_i32 s2, s20, s1
	s_add_i32 s3, s2, 0x1adf
	v_rcp_iflag_f32_e32 v1, v1
	s_sub_i32 s2, 0xffffe521, s2
	s_xor_b32 s14, s3, s20
	s_sub_i32 s5, 0, s4
	v_mul_f32_e32 v1, 0x4f7ffffe, v1
	v_cvt_u32_f32_e32 v1, v1
	s_max_i32 s2, s3, s2
	s_ashr_i32 s3, s14, 31
	v_readfirstlane_b32 s14, v1
	s_mul_i32 s5, s5, s14
	s_mul_hi_u32 s5, s14, s5
	s_add_i32 s14, s14, s5
	s_mul_hi_u32 s5, s2, s14
	s_mul_i32 s14, s5, s4
	s_sub_i32 s2, s2, s14
	s_add_i32 s14, s5, 1
	s_sub_i32 s15, s2, s4
	s_cmp_ge_u32 s2, s4
	s_cselect_b32 s5, s14, s5
	s_cselect_b32 s2, s15, s2
	s_add_i32 s14, s5, 1
	s_cmp_ge_u32 s2, s4
	s_cselect_b32 s2, s14, s5
	s_xor_b32 s2, s2, s3
	s_sub_i32 s29, s2, s3
	s_lshl_b32 s21, s29, 2
	s_add_i32 s22, s21, -1
	s_cmp_gt_i32 s29, 0
	s_cselect_b64 s[2:3], -1, 0
	s_and_b64 s[4:5], s[2:3], exec
	s_cselect_b32 s18, 0, s22
	s_ashr_i32 s4, s18, 2
	s_mul_i32 s17, s4, s20
	s_add_i32 s17, s17, s1
	s_cmpk_gt_i32 s17, 0x1fff
	s_mov_b32 s5, 0
	s_cbranch_scc0 .LBB0_91
	s_add_i32 s4, s17, 0xffffe000
	s_lshr_b32 s4, s4, 7
	s_lshl_b64 s[4:5], s[4:5], 24
	s_waitcnt lgkmcnt(0)
	s_add_u32 s14, s12, s4
	s_addc_u32 s15, s13, s5
	s_lshl_b32 s4, s17, 4
	s_and_b32 s26, s4, 0x780
	s_lshl_b32 s4, s17, 8
	s_and_b32 s16, s4, 0x700
	s_mov_b64 s[4:5], 0x800
	s_cbranch_execz .LBB0_92
	s_branch .LBB0_93

.LBB0_160:
	s_add_i32 s89, s59, -1
	s_cmp_lt_u32 s89, 8
	s_cselect_b32 s88, 1, 0
	s_cbranch_scc0 .Lp1c_skip1
	s_and_b32 s90, s89, 1
	s_lshr_b32 s91, s57, 2
	s_cmp_eq_u32 s90, s91
	s_cselect_b32 s88, 1, 0
	s_cbranch_scc0 .Lp1c_skip1
	s_lshr_b32 s89, s89, 1
	s_mul_i32 s89, s89, 200
	s_add_u32 s89, s89, s78
	s_add_u32 s89, s89, 6880
	s_cmp_lt_u32 s89, 0x2000
	s_cselect_b32 s88, 1, 0
	s_cbranch_scc0 .Lp1c_skip1
	s_lshr_b32 s90, s89, 4
	s_lshl_b32 s90, s90, 21
	s_and_b32 s91, s89, 15
	s_lshl_b32 s92, s91, 10
	s_or_b32 s90, s90, s92
	s_lshl_b32 s92, s57, 7
	s_or_b32 s90, s90, s92
	s_add_u32 s84, s82, s90
	s_addc_u32 s85, s83, 0
	s_lshr_b32 s90, s89, 8
	s_lshl_b32 s90, s90, 23
	s_lshl_b32 s91, s91, 19
	s_or_b32 s90, s90, s91
	s_bfe_u32 s91, s89, 0x40004
	s_lshl_b32 s91, s91, 7
	s_or_b32 s90, s90, s91
	s_lshl_b32 s91, s57, 15
	s_or_b32 s90, s90, s91
	s_add_u32 s90, s90, 0x4ee00000
	s_add_u32 s86, s48, s90
	s_addc_u32 s87, s49, 0
	global_load_dwordx4 v[180:183], v245, s[84:85] nt
	s_add_u32 s84, s84, 0x4000
	s_addc_u32 s85, s85, 0
	global_load_dwordx4 v[184:187], v245, s[84:85] nt
	s_add_u32 s84, s84, 0x4000
	s_addc_u32 s85, s85, 0
	global_load_dwordx4 v[188:191], v245, s[84:85] nt
	s_add_u32 s84, s84, 0x4000
	s_addc_u32 s85, s85, 0
	global_load_dwordx4 v[192:195], v245, s[84:85] nt
	s_add_u32 s84, s84, 0x4000
	s_addc_u32 s85, s85, 0
	global_load_dwordx4 v[196:199], v245, s[84:85] nt
	s_add_u32 s84, s84, 0x4000
	s_addc_u32 s85, s85, 0
	global_load_dwordx4 v[200:203], v245, s[84:85] nt
	s_add_u32 s84, s84, 0x4000
	s_addc_u32 s85, s85, 0
	global_load_dwordx4 v[204:207], v245, s[84:85] nt
	s_add_u32 s84, s84, 0x4000
	s_addc_u32 s85, s85, 0
	global_load_dwordx4 v[208:211], v245, s[84:85] nt
	s_add_u32 s84, s84, 0x4000
	s_addc_u32 s85, s85, 0
	global_load_dwordx4 v[212:215], v245, s[84:85] nt
	s_add_u32 s84, s84, 0x4000
	s_addc_u32 s85, s85, 0
	global_load_dwordx4 v[216:219], v245, s[84:85] nt
	s_add_u32 s84, s84, 0x4000
	s_addc_u32 s85, s85, 0
	global_load_dwordx4 v[220:223], v245, s[84:85] nt
	s_add_u32 s84, s84, 0x4000
	s_addc_u32 s85, s85, 0
	global_load_dwordx4 v[224:227], v245, s[84:85] nt
	s_add_u32 s84, s84, 0x4000
	s_addc_u32 s85, s85, 0
	global_load_dwordx4 v[228:231], v245, s[84:85] nt
	s_add_u32 s84, s84, 0x4000
	s_addc_u32 s85, s85, 0
	global_load_dwordx4 v[232:235], v245, s[84:85] nt
	s_add_u32 s84, s84, 0x4000
	s_addc_u32 s85, s85, 0
	global_load_dwordx4 v[236:239], v245, s[84:85] nt
	s_add_u32 s84, s84, 0x4000
	s_addc_u32 s85, s85, 0
	global_load_dwordx4 v[240:243], v245, s[84:85] nt

.LBB0_524:
	s_load_dwordx2 s[82:83], s[80:81], 0x78
	v_and_b32_e32 v245, 7, v162
	v_lshrrev_b32_e32 v246, 3, v162
	v_lshlrev_b32_e32 v244, 5, v245
	v_lshl_add_u32 v244, v246, 2, v244
	v_lshlrev_b32_e32 v247, 4, v245
	v_lshl_add_u32 v245, v246, 18, v247
	v_lshl_add_u32 v246, v246, 12, v247
	v_mov_b32_e32 v248, 0x42000000
	v_mov_b32_e32 v249, 0x42000000
	s_waitcnt lgkmcnt(0)
	s_add_u32 s10, s2, 0x22600000
	s_addc_u32 s11, s3, 0
	s_lshl_b32 s2, s12, 5
	s_add_i32 s59, s31, 0x18000
	s_mov_b64 s[12:13], 0x80
	s_and_b32 s18, s2, 0x60
	v_lshl_add_u64 v[8:9], v[8:9], 0, s[12:13]
	s_mov_b32 m0, s59
	s_add_i32 s60, s31, 0x1a000
	s_lshl_b32 s17, s16, 13
	s_lshl_b32 s19, s18, 7
	s_waitcnt vmcnt(2)
	s_barrier
	global_load_lds_dwordx4 v[8:9], off
	v_lshl_add_u64 v[4:5], v[4:5], 0, s[12:13]
	s_mov_b32 m0, s60
	s_add_i32 s61, s31, 0x8000
	s_add_i32 s62, s31, 0xa000
	global_load_lds_dwordx4 v[4:5], off
	v_lshl_add_u64 v[2:3], v[2:3], 0, s[12:13]
	s_mov_b32 m0, s61
	s_add_u32 s2, s36, 0x80080
	global_load_lds_dwordx4 v[2:3], off
	v_lshl_add_u64 v[2:3], v[6:7], 0, s[12:13]
	s_mov_b32 m0, s62
	s_addc_u32 s3, s37, 0
	s_add_i32 s63, s31, 0x1c000
	global_load_lds_dwordx4 v[2:3], off
	v_lshl_add_u64 v[2:3], s[2:3], 0, v[130:131]
	s_mov_b32 m0, s63
	s_add_i32 s64, s31, 0x1e000
	global_load_lds_dwordx4 v[2:3], off
	v_lshl_add_u64 v[2:3], s[2:3], 0, v[136:137]
	s_mov_b32 m0, s64
	v_lshlrev_b32_e32 v4, 6, v0
	global_load_lds_dwordx4 v[2:3], off
	v_and_b32_e32 v2, 15, v0
	v_lshlrev_b32_e32 v3, 1, v13
	s_movk_i32 s2, 0x3c0
	v_lshl_or_b32 v1, s16, 6, v2
	v_lshl_or_b32 v2, v2, 6, v3
	v_and_or_b32 v3, v4, s2, v3
	v_lshlrev_b32_e32 v4, 2, v0
	v_and_b32_e32 v4, 32, v4
	s_add_i32 s2, s19, 0
	v_xad_u32 v3, v3, v4, s2
	v_add_u32_e32 v152, 0x10000, v3
	v_add_u32_e32 v153, 0x14000, v3
	v_add_u32_e32 v154, 0x18000, v3
	v_add_u32_e32 v155, 0x1c000, v3
	v_add_u32_e32 v156, 0x10400, v3
	v_add_u32_e32 v157, 0x10800, v3
	v_add_u32_e32 v158, 0x10c00, v3
	v_add_u32_e32 v159, 0x14400, v3
	v_add_u32_e32 v160, 0x14800, v3
	v_add_u32_e32 v161, 0x14c00, v3
	v_add_u32_e32 v163, 0x18400, v3
	v_add_u32_e32 v164, 0x18800, v3
	v_add_u32_e32 v165, 0x18c00, v3
	v_add_u32_e32 v166, 0x1c400, v3
	v_add_u32_e32 v167, 0x1c800, v3
	v_add_u32_e32 v168, 0x1cc00, v3
	v_lshlrev_b32_e32 v3, 9, v0
	v_xad_u32 v2, v2, v4, 0
	v_and_b32_e32 v3, 0x30000, v3
	v_lshlrev_b32_e32 v4, 12, v12
	v_or3_b32 v3, v10, v3, v4
	v_add_u32_e32 v3, v3, v11
	v_or_b32_e32 v142, 0x80000, v3
	v_lshlrev_b32_e32 v3, 5, v14
	v_and_b32_e32 v3, 0x70000, v3
	s_waitcnt vmcnt(6)
	v_or3_b32 v3, v10, v3, v4
	s_cmpk_lt_u32 s15, 0x100
	v_add_u32_e32 v3, v3, v11
	v_mov_b32_e32 v135, v131
	v_mov_b32_e32 v141, v131
	s_sext_i32_i8 s69, s14
	s_cselect_b64 s[14:15], -1, 0
	s_ashr_i32 s65, s56, 31
	v_or_b32_e32 v169, s18, v13
	v_mov_b32_e32 v143, v131
	v_or_b32_e32 v144, 0x80000, v3
	v_mov_b32_e32 v145, v131
	v_mov_b64_e32 v[146:147], 0x200
	v_mov_b64_e32 v[148:149], 0x1ff
	v_add_u32_e32 v170, s17, v2
	s_mov_b64 s[16:17], 0x90000
	s_mov_b32 s66, 0x90000
	s_mov_b64 s[18:19], 0xa0000
	s_mov_b32 s67, 0xa0000
	s_mov_b64 s[20:21], 0xb0000
	s_mov_b32 s68, 0xb0000
	s_barrier
	s_branch .LBB0_527

.LBB0_537:
	s_add_i32 s89, s58, -1
	s_cmp_lt_u32 s89, 2
	s_cselect_b32 s88, 1, 0
	s_cbranch_scc0 .Lp4c_skip1
	s_mul_i32 s89, s89, 256
	s_add_u32 s89, s89, s78
	s_add_u32 s89, s89, 7680
	s_cmp_lt_u32 s89, 0x2000
	s_cselect_b32 s88, 1, 0
	s_cbranch_scc0 .Lp4c_skip1
	s_lshr_b32 s90, s89, 4
	s_lshl_b32 s90, s90, 21
	s_and_b32 s91, s89, 15
	s_lshl_b32 s92, s91, 10
	s_or_b32 s90, s90, s92
	s_lshl_b32 s92, s57, 7
	s_or_b32 s90, s90, s92
	s_add_u32 s84, s82, s90
	s_addc_u32 s85, s83, 0
	s_lshr_b32 s90, s89, 8
	s_lshl_b32 s90, s90, 23
	s_lshl_b32 s91, s91, 19
	s_or_b32 s90, s90, s91
	s_bfe_u32 s91, s89, 0x40004
	s_lshl_b32 s91, s91, 7
	s_or_b32 s90, s90, s91
	s_lshl_b32 s91, s57, 15
	s_or_b32 s90, s90, s91
	s_add_u32 s90, s90, 0x4ee00000
	s_add_u32 s86, s48, s90
	s_addc_u32 s87, s49, 0
	global_load_dwordx4 v[180:183], v245, s[84:85] nt
	s_add_u32 s84, s84, 0x4000
	s_addc_u32 s85, s85, 0
	global_load_dwordx4 v[184:187], v245, s[84:85] nt
	s_add_u32 s84, s84, 0x4000
	s_addc_u32 s85, s85, 0
	global_load_dwordx4 v[188:191], v245, s[84:85] nt
	s_add_u32 s84, s84, 0x4000
	s_addc_u32 s85, s85, 0
	global_load_dwordx4 v[192:195], v245, s[84:85] nt
	s_add_u32 s84, s84, 0x4000
	s_addc_u32 s85, s85, 0
	global_load_dwordx4 v[196:199], v245, s[84:85] nt
	s_add_u32 s84, s84, 0x4000
	s_addc_u32 s85, s85, 0
	global_load_dwordx4 v[200:203], v245, s[84:85] nt
	s_add_u32 s84, s84, 0x4000
	s_addc_u32 s85, s85, 0
	global_load_dwordx4 v[204:207], v245, s[84:85] nt
	s_add_u32 s84, s84, 0x4000
	s_addc_u32 s85, s85, 0
	global_load_dwordx4 v[208:211], v245, s[84:85] nt
	s_add_u32 s84, s84, 0x4000
	s_addc_u32 s85, s85, 0
	global_load_dwordx4 v[212:215], v245, s[84:85] nt
	s_add_u32 s84, s84, 0x4000
	s_addc_u32 s85, s85, 0
	global_load_dwordx4 v[216:219], v245, s[84:85] nt
	s_add_u32 s84, s84, 0x4000
	s_addc_u32 s85, s85, 0
	global_load_dwordx4 v[220:223], v245, s[84:85] nt
	s_add_u32 s84, s84, 0x4000
	s_addc_u32 s85, s85, 0
	global_load_dwordx4 v[224:227], v245, s[84:85] nt
	s_add_u32 s84, s84, 0x4000
	s_addc_u32 s85, s85, 0
	global_load_dwordx4 v[228:231], v245, s[84:85] nt
	s_add_u32 s84, s84, 0x4000
	s_addc_u32 s85, s85, 0
	global_load_dwordx4 v[232:235], v245, s[84:85] nt
	s_add_u32 s84, s84, 0x4000
	s_addc_u32 s85, s85, 0
	global_load_dwordx4 v[236:239], v245, s[84:85] nt
	s_add_u32 s84, s84, 0x4000
	s_addc_u32 s85, s85, 0
	global_load_dwordx4 v[240:243], v245, s[84:85] nt
.Lp4c_skip1:
	v_lshl_add_u32 v172, s30, 8, v1
	v_lshl_or_b32 v150, s69, 8, v169
	v_ashrrev_i32_e32 v173, 31, v172
	v_ashrrev_i32_e32 v151, 31, v150
	v_lshlrev_b64 v[174:175], 12, v[172:173]
	v_lshl_add_u64 v[174:175], s[10:11], 0, v[174:175]
	v_lshlrev_b64 v[176:177], 1, v[150:151]
	v_lshl_add_u64 v[150:151], v[174:175], 0, v[176:177]
	v_cvt_pk_bf16_f32 v126, v126, v127
	v_cvt_pk_bf16_f32 v127, v128, v129
	v_cvt_pk_bf16_f32 v128, v122, v123
	v_cvt_pk_bf16_f32 v129, v124, v125
	global_store_dwordx4 v[150:151], v[126:129], off
	v_cvt_pk_bf16_f32 v114, v114, v115
	v_cvt_pk_bf16_f32 v115, v116, v117
	v_cvt_pk_bf16_f32 v116, v106, v107
	v_or_b32_e32 v106, 16, v172
	v_ashrrev_i32_e32 v107, 31, v106
	v_lshlrev_b64 v[106:107], 12, v[106:107]
	v_lshl_add_u64 v[106:107], s[10:11], 0, v[106:107]
	v_cvt_pk_bf16_f32 v117, v108, v109
	global_store_dwordx4 v[150:151], v[114:117], off offset:256
	s_nop 1
	v_lshl_add_u64 v[114:115], v[106:107], 0, v[176:177]
	v_cvt_pk_bf16_f32 v106, v118, v119
	v_cvt_pk_bf16_f32 v107, v120, v121
	v_cvt_pk_bf16_f32 v108, v110, v111
	v_cvt_pk_bf16_f32 v109, v112, v113
	global_store_dwordx4 v[114:115], v[106:109], off
	v_cvt_pk_bf16_f32 v98, v98, v99
	v_cvt_pk_bf16_f32 v99, v100, v101
	v_cvt_pk_bf16_f32 v100, v90, v91
	v_or_b32_e32 v90, 32, v172
	v_ashrrev_i32_e32 v91, 31, v90
	v_lshlrev_b64 v[90:91], 12, v[90:91]
	v_lshl_add_u64 v[90:91], s[10:11], 0, v[90:91]
	v_cvt_pk_bf16_f32 v101, v92, v93
	global_store_dwordx4 v[114:115], v[98:101], off offset:256
	s_nop 1
	v_lshl_add_u64 v[98:99], v[90:91], 0, v[176:177]
	v_cvt_pk_bf16_f32 v90, v102, v103
	v_cvt_pk_bf16_f32 v91, v104, v105
	v_cvt_pk_bf16_f32 v92, v94, v95
	v_cvt_pk_bf16_f32 v93, v96, v97
	global_store_dwordx4 v[98:99], v[90:93], off
	v_cvt_pk_bf16_f32 v82, v82, v83
	v_cvt_pk_bf16_f32 v83, v84, v85
	v_cvt_pk_bf16_f32 v84, v74, v75
	v_or_b32_e32 v74, 48, v172
	v_ashrrev_i32_e32 v75, 31, v74
	v_lshlrev_b64 v[74:75], 12, v[74:75]
	v_lshl_add_u64 v[74:75], s[10:11], 0, v[74:75]
	v_cvt_pk_bf16_f32 v85, v76, v77
	global_store_dwordx4 v[98:99], v[82:85], off offset:256
	s_nop 1
	v_lshl_add_u64 v[82:83], v[74:75], 0, v[176:177]
	v_cvt_pk_bf16_f32 v74, v86, v87
	v_cvt_pk_bf16_f32 v75, v88, v89
	v_cvt_pk_bf16_f32 v76, v78, v79
	v_cvt_pk_bf16_f32 v77, v80, v81
	global_store_dwordx4 v[82:83], v[74:77], off
	v_cvt_pk_bf16_f32 v70, v70, v71
	v_cvt_pk_bf16_f32 v71, v72, v73
	v_cvt_pk_bf16_f32 v72, v66, v67
	v_cvt_pk_bf16_f32 v73, v68, v69
	global_store_dwordx4 v[82:83], v[70:73], off offset:256
	v_cvt_pk_bf16_f32 v62, v62, v63
	v_cvt_pk_bf16_f32 v63, v64, v65
	v_cvt_pk_bf16_f32 v64, v58, v59
	v_add_co_u32_e32 v58, vcc, s55, v150
	v_lshl_add_u64 v[66:67], v[150:151], 0, s[6:7]
	s_nop 0
	v_addc_co_u32_e32 v59, vcc, 0, v151, vcc
	v_cvt_pk_bf16_f32 v65, v60, v61
	global_store_dwordx4 v[58:59], v[62:65], off
	v_cvt_pk_bf16_f32 v42, v42, v43
	v_cvt_pk_bf16_f32 v43, v44, v45
	v_cvt_pk_bf16_f32 v44, v30, v31
	v_cvt_pk_bf16_f32 v45, v32, v33
	global_store_dwordx4 v[66:67], v[42:45], off offset:256
	v_cvt_pk_bf16_f32 v30, v46, v47
	v_cvt_pk_bf16_f32 v31, v48, v49
	v_cvt_pk_bf16_f32 v32, v38, v39
	v_add_co_u32_e32 v38, vcc, s66, v150
	s_nop 0
	v_lshl_add_u64 v[42:43], v[150:151], 0, s[16:17]
	v_addc_co_u32_e32 v39, vcc, 0, v151, vcc
	v_cvt_pk_bf16_f32 v33, v40, v41
	global_store_dwordx4 v[38:39], v[30:33], off
	v_cvt_pk_bf16_f32 v18, v18, v19
	v_cvt_pk_bf16_f32 v19, v20, v21
	v_cvt_pk_bf16_f32 v20, v10, v11
	v_cvt_pk_bf16_f32 v21, v12, v13
	global_store_dwordx4 v[42:43], v[18:21], off offset:256
	v_cvt_pk_bf16_f32 v10, v22, v23
	v_cvt_pk_bf16_f32 v11, v24, v25
	v_cvt_pk_bf16_f32 v12, v14, v15
	v_add_co_u32_e32 v14, vcc, s67, v150
	s_nop 0
	v_lshl_add_u64 v[18:19], v[150:151], 0, s[18:19]
	v_cvt_pk_bf16_f32 v13, v16, v17
	v_addc_co_u32_e32 v15, vcc, 0, v151, vcc
	global_store_dwordx4 v[14:15], v[10:13], off
	s_nop 1
	v_cvt_pk_bf16_f32 v10, v54, v55
	v_cvt_pk_bf16_f32 v11, v56, v57
	v_cvt_pk_bf16_f32 v12, v50, v51
	v_cvt_pk_bf16_f32 v13, v52, v53
	global_store_dwordx4 v[18:19], v[10:13], off offset:256
	v_cvt_pk_bf16_f32 v6, v6, v7
	v_cvt_pk_bf16_f32 v7, v8, v9
	v_cvt_pk_bf16_f32 v8, v2, v3
	v_add_co_u32_e32 v2, vcc, s68, v150
	s_nop 0
	v_lshl_add_u64 v[10:11], v[150:151], 0, s[20:21]
	v_addc_co_u32_e32 v3, vcc, 0, v151, vcc
	s_andn2_b64 vcc, exec, s[2:3]
	s_mov_b64 s[2:3], -1
	v_cvt_pk_bf16_f32 v9, v4, v5
	global_store_dwordx4 v[2:3], v[6:9], off
	v_cvt_pk_bf16_f32 v2, v34, v35
	v_cvt_pk_bf16_f32 v3, v36, v37
	v_cvt_pk_bf16_f32 v4, v26, v27
	v_cvt_pk_bf16_f32 v5, v28, v29
	global_store_dwordx4 v[10:11], v[2:5], off offset:256
	s_cmp_eq_u32 s88, 0
	s_cbranch_scc1 .Lp4c_skip3
	s_waitcnt vmcnt(16)
	v_pk_mul_f32 v[180:181], v[180:181], v[248:249]
	v_pk_mul_f32 v[182:183], v[182:183], v[248:249]
	v_pk_mul_f32 v[184:185], v[184:185], v[248:249]
	v_pk_mul_f32 v[186:187], v[186:187], v[248:249]
	v_pk_mul_f32 v[188:189], v[188:189], v[248:249]
	v_pk_mul_f32 v[190:191], v[190:191], v[248:249]
	v_pk_mul_f32 v[192:193], v[192:193], v[248:249]
	v_pk_mul_f32 v[194:195], v[194:195], v[248:249]
	v_pk_mul_f32 v[196:197], v[196:197], v[248:249]
	v_pk_mul_f32 v[198:199], v[198:199], v[248:249]
	v_pk_mul_f32 v[200:201], v[200:201], v[248:249]
	v_pk_mul_f32 v[202:203], v[202:203], v[248:249]
	v_pk_mul_f32 v[204:205], v[204:205], v[248:249]
	v_pk_mul_f32 v[206:207], v[206:207], v[248:249]
	v_pk_mul_f32 v[208:209], v[208:209], v[248:249]
	v_pk_mul_f32 v[210:211], v[210:211], v[248:249]
	v_pk_mul_f32 v[212:213], v[212:213], v[248:249]
	v_pk_mul_f32 v[214:215], v[214:215], v[248:249]
	v_pk_mul_f32 v[216:217], v[216:217], v[248:249]
	v_pk_mul_f32 v[218:219], v[218:219], v[248:249]
	v_pk_mul_f32 v[220:221], v[220:221], v[248:249]
	v_pk_mul_f32 v[222:223], v[222:223], v[248:249]
	v_pk_mul_f32 v[224:225], v[224:225], v[248:249]
	v_pk_mul_f32 v[226:227], v[226:227], v[248:249]
	v_pk_mul_f32 v[228:229], v[228:229], v[248:249]
	v_pk_mul_f32 v[230:231], v[230:231], v[248:249]
	v_pk_mul_f32 v[232:233], v[232:233], v[248:249]
	v_pk_mul_f32 v[234:235], v[234:235], v[248:249]
	v_pk_mul_f32 v[236:237], v[236:237], v[248:249]
	v_pk_mul_f32 v[238:239], v[238:239], v[248:249]
	v_pk_mul_f32 v[240:241], v[240:241], v[248:249]
	v_pk_mul_f32 v[242:243], v[242:243], v[248:249]
	v_cvt_pk_fp8_f32 v34, v180, v184
	v_cvt_pk_fp8_f32 v35, v196, v200
	v_cvt_pk_fp8_f32 v36, v212, v216
	v_cvt_pk_fp8_f32 v37, v228, v232
	v_cvt_pk_fp8_f32 v34, v188, v192 op_sel:[0,0,1]
	v_cvt_pk_fp8_f32 v35, v204, v208 op_sel:[0,0,1]
	v_cvt_pk_fp8_f32 v36, v220, v224 op_sel:[0,0,1]
	v_cvt_pk_fp8_f32 v37, v236, v240 op_sel:[0,0,1]
	v_cvt_pk_fp8_f32 v38, v181, v185
	v_cvt_pk_fp8_f32 v39, v197, v201
	v_cvt_pk_fp8_f32 v40, v213, v217
	v_cvt_pk_fp8_f32 v41, v229, v233
	v_cvt_pk_fp8_f32 v38, v189, v193 op_sel:[0,0,1]
	v_cvt_pk_fp8_f32 v39, v205, v209 op_sel:[0,0,1]
	v_cvt_pk_fp8_f32 v40, v221, v225 op_sel:[0,0,1]
	v_cvt_pk_fp8_f32 v41, v237, v241 op_sel:[0,0,1]
	v_cvt_pk_fp8_f32 v42, v182, v186
	v_cvt_pk_fp8_f32 v43, v198, v202
	v_cvt_pk_fp8_f32 v44, v214, v218
	v_cvt_pk_fp8_f32 v45, v230, v234
	v_cvt_pk_fp8_f32 v42, v190, v194 op_sel:[0,0,1]
	v_cvt_pk_fp8_f32 v43, v206, v210 op_sel:[0,0,1]
	v_cvt_pk_fp8_f32 v44, v222, v226 op_sel:[0,0,1]
	v_cvt_pk_fp8_f32 v45, v238, v242 op_sel:[0,0,1]
	v_cvt_pk_fp8_f32 v46, v183, v187
	v_cvt_pk_fp8_f32 v47, v199, v203
	v_cvt_pk_fp8_f32 v48, v215, v219
	v_cvt_pk_fp8_f32 v49, v231, v235
	v_cvt_pk_fp8_f32 v46, v191, v195 op_sel:[0,0,1]
	v_cvt_pk_fp8_f32 v47, v207, v211 op_sel:[0,0,1]
	v_cvt_pk_fp8_f32 v48, v223, v227 op_sel:[0,0,1]
	v_cvt_pk_fp8_f32 v49, v239, v243 op_sel:[0,0,1]
	s_nop 1
	ds_bpermute_b32 v50, v244, v34
	ds_bpermute_b32 v51, v244, v35
	ds_bpermute_b32 v52, v244, v36
	ds_bpermute_b32 v53, v244, v37
	ds_bpermute_b32 v54, v244, v38
	ds_bpermute_b32 v55, v244, v39
	ds_bpermute_b32 v56, v244, v40
	ds_bpermute_b32 v57, v244, v41
	ds_bpermute_b32 v58, v244, v42
	ds_bpermute_b32 v59, v244, v43
	ds_bpermute_b32 v60, v244, v44
	ds_bpermute_b32 v61, v244, v45
	ds_bpermute_b32 v62, v244, v46
	ds_bpermute_b32 v63, v244, v47
	ds_bpermute_b32 v64, v244, v48
	ds_bpermute_b32 v65, v244, v49
	s_waitcnt lgkmcnt(0)
	global_store_dwordx4 v246, v[50:53], s[86:87] nt
	s_add_u32 s90, s86, 0x40000
	s_addc_u32 s91, s87, 0
	global_store_dwordx4 v246, v[54:57], s[90:91] nt
	s_add_u32 s90, s86, 0x800
	s_addc_u32 s91, s87, 0
	global_store_dwordx4 v246, v[58:61], s[90:91] nt
	s_add_u32 s90, s86, 0x40800
	s_addc_u32 s91, s87, 0
	global_store_dwordx4 v246, v[62:65], s[90:91] nt
.Lp4c_skip3:
	s_cbranch_vccnz .LBB0_526
	s_andn2_b64 vcc, exec, s[8:9]
	s_cbranch_vccnz .LBB0_525
	s_barrier
	s_branch .LBB0_525
